# U sweep gather ring deepened from 3 to 6 batches in flight (12 loads per wave), er in s10-s15
# speedup vs baseline: 1.0012x; 1.0012x over previous
; #define LAS __attribute__((address_space(3)))
; #define LDS_WAIT() asm volatile("s_waitcnt lgkmcnt(0)" ::: "memory")
; #define PE_ISSUE_U(S, rec_) PE_ISSUE4(S, rec_, UB8)
;     ...
;     if (lane < 2 * PE_RD_N) *(LAS v4u*)(ents + 4 * (nb + lane)) = (v4u){0u, 0u, 0u, 0u};
;     LDS_WAIT(); asm volatile("" ::: "memory");
;     ...
;     {
;         unsigned er[PE_RD];
; #pragma unroll
;         for (int q = 0; q < PE_RD; ++q) { const v4u rec = *(const LAS v4u*)(ents + 4 * q); er[q] = __builtin_amdgcn_readfirstlane(rec.x); PE_ISSUE_U(q, rec); }
;         int jcur = (int)((er[0] >> 14) & 3u);
;         v4u hcur = *(const LAS v4u*)(hql + (jcur * 64 + lane) * 4);
;         v4u nrec = *(const LAS v4u*)(ents + 4 * PE_RD);
; #pragma unroll 1
.LBB0_2832:
	s_or_b64 exec, exec, s[0:1]
	v_cmp_gt_i32_e32 vcc, 12, v50
	s_and_saveexec_b64 s[0:1], vcc
	v_add_u32_e32 v0, s6, v50
	v_lshl_add_u32 v0, v0, 4, s90
	ds_write_b128 v0, v[122:125] offset:6720
	s_or_b64 exec, exec, s[0:1]
	s_waitcnt lgkmcnt(0)
	v_mov_b32_e32 v5, s90
	ds_read_b128 v[0:3], v5 offset:6720
	v_lshlrev_b32_e32 v118, 3, v50
	v_and_b32_e32 v43, 31, v50
	v_cmp_lt_u32_e64 s[100:101], 31, v50
	v_lshlrev_b32_e32 v43, 4, v43
	v_lshl_add_u32 v52, v43, 1, s90
	s_cmp_gt_i32 s6, 0
	s_cselect_b64 s[2:3], -1, 0
	s_waitcnt lgkmcnt(0)
	v_readfirstlane_b32 s10, v0
	v_and_b32_e32 v48, 0x3fff, v0
	v_cndmask_b32_e64 v48, v48, v1, s[100:101]
	v_lshl_add_u32 v48, v48, 9, v43
	global_load_dwordx4 v[8:11], v48, s[70:71]
	v_cndmask_b32_e64 v48, v2, v3, s[100:101]
	v_lshl_add_u32 v48, v48, 9, v43
	global_load_dwordx4 v[12:15], v48, s[70:71]
	ds_read_b128 v[0:3], v5 offset:6736
	s_waitcnt lgkmcnt(0)
	v_readfirstlane_b32 s11, v0
	v_and_b32_e32 v48, 0x3fff, v0
	v_cndmask_b32_e64 v48, v48, v1, s[100:101]
	v_lshl_add_u32 v48, v48, 9, v43
	global_load_dwordx4 v[16:19], v48, s[70:71]
	v_cndmask_b32_e64 v48, v2, v3, s[100:101]
	v_lshl_add_u32 v48, v48, 9, v43
	global_load_dwordx4 v[20:23], v48, s[70:71]
	ds_read_b128 v[0:3], v5 offset:6752
	s_waitcnt lgkmcnt(0)
	v_readfirstlane_b32 s12, v0
	v_and_b32_e32 v48, 0x3fff, v0
	v_cndmask_b32_e64 v48, v48, v1, s[100:101]
	v_lshl_add_u32 v48, v48, 9, v43
	global_load_dwordx4 v[24:27], v48, s[70:71]
	v_cndmask_b32_e64 v48, v2, v3, s[100:101]
	v_lshl_add_u32 v48, v48, 9, v43
	global_load_dwordx4 v[28:31], v48, s[70:71]
	ds_read_b128 v[0:3], v5 offset:6768
	s_waitcnt lgkmcnt(0)
	v_readfirstlane_b32 s13, v0
	v_and_b32_e32 v48, 0x3fff, v0
	v_cndmask_b32_e64 v48, v48, v1, s[100:101]
	v_lshl_add_u32 v48, v48, 9, v43
	global_load_dwordx4 v[56:59], v48, s[70:71]
	v_cndmask_b32_e64 v48, v2, v3, s[100:101]
	v_lshl_add_u32 v48, v48, 9, v43
	global_load_dwordx4 v[60:63], v48, s[70:71]
	ds_read_b128 v[0:3], v5 offset:6784
	s_waitcnt lgkmcnt(0)
	v_readfirstlane_b32 s14, v0
	v_and_b32_e32 v48, 0x3fff, v0
	v_cndmask_b32_e64 v48, v48, v1, s[100:101]
	v_lshl_add_u32 v48, v48, 9, v43
	global_load_dwordx4 v[64:67], v48, s[70:71]
	v_cndmask_b32_e64 v48, v2, v3, s[100:101]
	v_lshl_add_u32 v48, v48, 9, v43
	global_load_dwordx4 v[68:71], v48, s[70:71]
	ds_read_b128 v[0:3], v5 offset:6800
	s_waitcnt lgkmcnt(0)
	v_readfirstlane_b32 s15, v0
	v_and_b32_e32 v48, 0x3fff, v0
	v_cndmask_b32_e64 v48, v48, v1, s[100:101]
	v_lshl_add_u32 v48, v48, 9, v43
	global_load_dwordx4 v[72:75], v48, s[70:71]
	v_cndmask_b32_e64 v48, v2, v3, s[100:101]
	v_lshl_add_u32 v48, v48, 9, v43
	global_load_dwordx4 v[76:79], v48, s[70:71]
	s_cmp_lt_i32 s6, 1
	s_cbranch_scc1 .LBB0_2861
	s_bfe_u32 s9, s10, 0x2000e
	v_lshl_add_u32 v48, s9, 10, v52
	ds_read_b128 v[0:3], v48 offset:11072
	ds_read_b128 v[44:47], v48 offset:11088
	v_and_b32_e32 v4, 15, v50
	v_bfe_u32 v33, v50, 4, 1
	v_cmp_eq_u32_e32 vcc, 0, v4
	v_lshrrev_b32_e32 v4, 5, v50
	s_mov_b32 s7, 0
	v_lshl_add_u32 v33, v33, 1, v4
	v_readlane_b32 s8, v255, 2
	s_nop 1
	s_add_i32 s8, s8, 48
	v_mov_b32_e32 v136, s8
	s_waitcnt lgkmcnt(0)
.LBB0_2838:
	ds_read_b128 v[4:7], v136
	s_waitcnt vmcnt(10)
	s_bfe_u32 s0, s10, 0x30010
	s_cmp_lg_u32 s0, 0
	s_cbranch_scc0 .Lu16_skip0
	s_bfe_u32 s1, s10, 0x2000e
	s_cmp_eq_u32 s1, s9
	s_cbranch_scc1 .Lu16_same0
	v_lshl_add_u32 v48, s1, 10, v52
	ds_read_b128 v[0:3], v48 offset:11072
	ds_read_b128 v[44:47], v48 offset:11088
	s_mov_b32 s9, s1
	s_waitcnt lgkmcnt(0)

; #define LAS __attribute__((address_space(3)))
; #define PE_VMW "vmcnt(" PE_STR(PE_VMY) ")"
; #define PE_ISSUE_U(S, rec_) PE_ISSUE4(S, rec_, UB8)
; #define PE_WAIT4U(S, cntstr) asm volatile("s_waitcnt " cntstr : "+v"(ru4[S][0]), "+v"(ru4[S][1]), "+v"(ru4[S][2]), "+v"(ru4[S][3]) :: "memory")
;     ...
; #pragma unroll
;             for (int q = 0; q < PE_RD; ++q) {
;                 PE_WAIT4U(q, PE_VMW);
;                 PE_UBATCH(q, er[q]);
;                 er[q] = __builtin_amdgcn_readfirstlane(nrec.x);
;                 PE_ISSUE_U(q, nrec);
;                 nrec = *(const LAS v4u*)(ents + 4 * (bi + q + PE_RD + 1));
.Lu16_skip0:
	s_waitcnt lgkmcnt(0)
	v_readfirstlane_b32 s10, v4
	v_and_b32_e32 v48, 0x3fff, v4
	v_cndmask_b32_e64 v48, v48, v5, s[100:101]
	v_lshl_add_u32 v48, v48, 9, v43
	global_load_dwordx4 v[8:11], v48, s[70:71]
	v_cndmask_b32_e64 v48, v6, v7, s[100:101]
	v_lshl_add_u32 v48, v48, 9, v43
	global_load_dwordx4 v[12:15], v48, s[70:71]
	ds_read_b128 v[4:7], v136 offset:16
	s_waitcnt vmcnt(10)
	s_bfe_u32 s0, s11, 0x30010
	s_cmp_lg_u32 s0, 0
	s_cbranch_scc0 .Lu16_skip1
	s_bfe_u32 s1, s11, 0x2000e
	s_cmp_eq_u32 s1, s9
	s_cbranch_scc1 .Lu16_same1
	v_lshl_add_u32 v48, s1, 10, v52
	ds_read_b128 v[0:3], v48 offset:11072
	ds_read_b128 v[44:47], v48 offset:11088
	s_mov_b32 s9, s1
	s_waitcnt lgkmcnt(0)

; #define LAS __attribute__((address_space(3)))
; #define PE_VMW "vmcnt(" PE_STR(PE_VMY) ")"
; #define PE_ISSUE_U(S, rec_) PE_ISSUE4(S, rec_, UB8)
; #define PE_WAIT4U(S, cntstr) asm volatile("s_waitcnt " cntstr : "+v"(ru4[S][0]), "+v"(ru4[S][1]), "+v"(ru4[S][2]), "+v"(ru4[S][3]) :: "memory")
;     ...
; #pragma unroll
;             for (int q = 0; q < PE_RD; ++q) {
;                 PE_WAIT4U(q, PE_VMW);
;                 PE_UBATCH(q, er[q]);
;                 er[q] = __builtin_amdgcn_readfirstlane(nrec.x);
;                 PE_ISSUE_U(q, nrec);
;                 nrec = *(const LAS v4u*)(ents + 4 * (bi + q + PE_RD + 1));
.Lu16_skip1:
	s_waitcnt lgkmcnt(0)
	v_readfirstlane_b32 s11, v4
	v_and_b32_e32 v48, 0x3fff, v4
	v_cndmask_b32_e64 v48, v48, v5, s[100:101]
	v_lshl_add_u32 v48, v48, 9, v43
	global_load_dwordx4 v[16:19], v48, s[70:71]
	v_cndmask_b32_e64 v48, v6, v7, s[100:101]
	v_lshl_add_u32 v48, v48, 9, v43
	global_load_dwordx4 v[20:23], v48, s[70:71]
	ds_read_b128 v[4:7], v136 offset:32
	s_waitcnt vmcnt(10)
	s_bfe_u32 s0, s12, 0x30010
	s_cmp_lg_u32 s0, 0
	s_cbranch_scc0 .Lu16_skip2
	s_bfe_u32 s1, s12, 0x2000e
	s_cmp_eq_u32 s1, s9
	s_cbranch_scc1 .Lu16_same2
	v_lshl_add_u32 v48, s1, 10, v52
	ds_read_b128 v[0:3], v48 offset:11072
	ds_read_b128 v[44:47], v48 offset:11088
	s_mov_b32 s9, s1
	s_waitcnt lgkmcnt(0)

; #define LAS __attribute__((address_space(3)))
; #define PE_VMW "vmcnt(" PE_STR(PE_VMY) ")"
; #define PE_ISSUE_U(S, rec_) PE_ISSUE4(S, rec_, UB8)
; #define PE_WAIT4U(S, cntstr) asm volatile("s_waitcnt " cntstr : "+v"(ru4[S][0]), "+v"(ru4[S][1]), "+v"(ru4[S][2]), "+v"(ru4[S][3]) :: "memory")
;     ...
; #pragma unroll
;             for (int q = 0; q < PE_RD; ++q) {
;                 PE_WAIT4U(q, PE_VMW);
;                 PE_UBATCH(q, er[q]);
;                 er[q] = __builtin_amdgcn_readfirstlane(nrec.x);
;                 PE_ISSUE_U(q, nrec);
;                 nrec = *(const LAS v4u*)(ents + 4 * (bi + q + PE_RD + 1));
;             }
.Lu16_skip2:
	s_waitcnt lgkmcnt(0)
	v_readfirstlane_b32 s12, v4
	v_and_b32_e32 v48, 0x3fff, v4
	v_cndmask_b32_e64 v48, v48, v5, s[100:101]
	v_lshl_add_u32 v48, v48, 9, v43
	global_load_dwordx4 v[24:27], v48, s[70:71]
	v_cndmask_b32_e64 v48, v6, v7, s[100:101]
	v_lshl_add_u32 v48, v48, 9, v43
	global_load_dwordx4 v[28:31], v48, s[70:71]
	ds_read_b128 v[4:7], v136 offset:48
	s_waitcnt vmcnt(10)
	s_bfe_u32 s0, s13, 0x30010
	s_cmp_lg_u32 s0, 0
	s_cbranch_scc0 .Lu16_skip3
	s_bfe_u32 s1, s13, 0x2000e
	s_cmp_eq_u32 s1, s9
	s_cbranch_scc1 .Lu16_same3
	v_lshl_add_u32 v48, s1, 10, v52
	ds_read_b128 v[0:3], v48 offset:11072
	ds_read_b128 v[44:47], v48 offset:11088
	s_mov_b32 s9, s1
	s_waitcnt lgkmcnt(0)
.Lu16_same3:
	v_dot8_i32_i4 v39, v56, v0, 0
	v_dot8_i32_i4 v40, v60, v0, 0
	v_dot8_i32_i4 v35, v56, v2, 0
	v_dot8_i32_i4 v36, v60, v2, 0
	v_dot8_i32_i4 v39, v57, v1, v39
	v_dot8_i32_i4 v40, v61, v1, v40
	v_dot8_i32_i4 v35, v57, v3, v35
	v_dot8_i32_i4 v36, v61, v3, v36
	v_dot8_i32_i4 v39, v58, v44, v39
	v_dot8_i32_i4 v40, v62, v44, v40
	v_dot8_i32_i4 v35, v58, v46, v35
	v_dot8_i32_i4 v36, v62, v46, v36
	v_dot8_i32_i4 v39, v59, v45, v39
	v_dot8_i32_i4 v40, v63, v45, v40
	v_dot8_i32_i4 v35, v59, v47, v35
	v_dot8_i32_i4 v36, v63, v47, v36
	s_nop 2
	v_lshl_add_u32 v39, v39, 4, v35
	v_lshl_add_u32 v40, v40, 4, v36
	s_mulk_i32 s1, 0x690
	s_nop 0
	v_permlane16_swap_b32_e32 v39, v40
	v_add_u32_e32 v39, v39, v40
	s_lshr_b32 s4, s13, 17
	s_add_i32 s1, s90, s1
	v_add_u32_dpp v39, v39, v39 quad_perm:[1,0,3,2] row_mask:0xf bank_mask:0xf bound_ctrl:1
	s_and_b32 s4, s4, 0x7ffc
	s_add_i32 s1, s1, s4
	v_add_u32_dpp v39, v39, v39 quad_perm:[2,3,0,1] row_mask:0xf bank_mask:0xf bound_ctrl:1
	v_lshl_add_u32 v34, v33, 2, s1
	s_nop 0
	v_add_u32_dpp v41, v39, v39 row_half_mirror row_mask:0xf bank_mask:0xf bound_ctrl:1
	s_nop 1
	v_mov_b32_dpp v42, v41 row_mirror row_mask:0xf bank_mask:0xf bound_ctrl:1
	v_add_u32_e32 v42, v41, v42
	s_and_saveexec_b64 s[0:1], vcc
	ds_write_b32 v34, v42
	s_or_b64 exec, exec, s[0:1]
.Lu16_skip3:
	s_waitcnt lgkmcnt(0)
	v_readfirstlane_b32 s13, v4
	v_and_b32_e32 v48, 0x3fff, v4
	v_cndmask_b32_e64 v48, v48, v5, s[100:101]
	v_lshl_add_u32 v48, v48, 9, v43
	global_load_dwordx4 v[56:59], v48, s[70:71]
	v_cndmask_b32_e64 v48, v6, v7, s[100:101]
	v_lshl_add_u32 v48, v48, 9, v43
	global_load_dwordx4 v[60:63], v48, s[70:71]
	ds_read_b128 v[4:7], v136 offset:64
	s_waitcnt vmcnt(10)
	s_bfe_u32 s0, s14, 0x30010
	s_cmp_lg_u32 s0, 0
	s_cbranch_scc0 .Lu16_skip4
	s_bfe_u32 s1, s14, 0x2000e
	s_cmp_eq_u32 s1, s9
	s_cbranch_scc1 .Lu16_same4
	v_lshl_add_u32 v48, s1, 10, v52
	ds_read_b128 v[0:3], v48 offset:11072
	ds_read_b128 v[44:47], v48 offset:11088
	s_mov_b32 s9, s1
	s_waitcnt lgkmcnt(0)
.Lu16_same4:
	v_dot8_i32_i4 v39, v64, v0, 0
	v_dot8_i32_i4 v40, v68, v0, 0
	v_dot8_i32_i4 v35, v64, v2, 0
	v_dot8_i32_i4 v36, v68, v2, 0
	v_dot8_i32_i4 v39, v65, v1, v39
	v_dot8_i32_i4 v40, v69, v1, v40
	v_dot8_i32_i4 v35, v65, v3, v35
	v_dot8_i32_i4 v36, v69, v3, v36
	v_dot8_i32_i4 v39, v66, v44, v39
	v_dot8_i32_i4 v40, v70, v44, v40
	v_dot8_i32_i4 v35, v66, v46, v35
	v_dot8_i32_i4 v36, v70, v46, v36
	v_dot8_i32_i4 v39, v67, v45, v39
	v_dot8_i32_i4 v40, v71, v45, v40
	v_dot8_i32_i4 v35, v67, v47, v35
	v_dot8_i32_i4 v36, v71, v47, v36
	s_nop 2
	v_lshl_add_u32 v39, v39, 4, v35
	v_lshl_add_u32 v40, v40, 4, v36
	s_mulk_i32 s1, 0x690
	s_nop 0
	v_permlane16_swap_b32_e32 v39, v40
	v_add_u32_e32 v39, v39, v40
	s_lshr_b32 s4, s14, 17
	s_add_i32 s1, s90, s1
	v_add_u32_dpp v39, v39, v39 quad_perm:[1,0,3,2] row_mask:0xf bank_mask:0xf bound_ctrl:1
	s_and_b32 s4, s4, 0x7ffc
	s_add_i32 s1, s1, s4
	v_add_u32_dpp v39, v39, v39 quad_perm:[2,3,0,1] row_mask:0xf bank_mask:0xf bound_ctrl:1
	v_lshl_add_u32 v34, v33, 2, s1
	s_nop 0
	v_add_u32_dpp v41, v39, v39 row_half_mirror row_mask:0xf bank_mask:0xf bound_ctrl:1
	s_nop 1
	v_mov_b32_dpp v42, v41 row_mirror row_mask:0xf bank_mask:0xf bound_ctrl:1
	v_add_u32_e32 v42, v41, v42
	s_and_saveexec_b64 s[0:1], vcc
	ds_write_b32 v34, v42
	s_or_b64 exec, exec, s[0:1]
.Lu16_skip4:
	s_waitcnt lgkmcnt(0)
	v_readfirstlane_b32 s14, v4
	v_and_b32_e32 v48, 0x3fff, v4
	v_cndmask_b32_e64 v48, v48, v5, s[100:101]
	v_lshl_add_u32 v48, v48, 9, v43
	global_load_dwordx4 v[64:67], v48, s[70:71]
	v_cndmask_b32_e64 v48, v6, v7, s[100:101]
	v_lshl_add_u32 v48, v48, 9, v43
	global_load_dwordx4 v[68:71], v48, s[70:71]
	ds_read_b128 v[4:7], v136 offset:80
	s_waitcnt vmcnt(10)
	s_bfe_u32 s0, s15, 0x30010
	s_cmp_lg_u32 s0, 0
	s_cbranch_scc0 .Lu16_skip5
	s_bfe_u32 s1, s15, 0x2000e
	s_cmp_eq_u32 s1, s9
	s_cbranch_scc1 .Lu16_same5
	v_lshl_add_u32 v48, s1, 10, v52
	ds_read_b128 v[0:3], v48 offset:11072
	ds_read_b128 v[44:47], v48 offset:11088
	s_mov_b32 s9, s1
	s_waitcnt lgkmcnt(0)
.Lu16_same5:
	v_dot8_i32_i4 v39, v72, v0, 0
	v_dot8_i32_i4 v40, v76, v0, 0
	v_dot8_i32_i4 v35, v72, v2, 0
	v_dot8_i32_i4 v36, v76, v2, 0
	v_dot8_i32_i4 v39, v73, v1, v39
	v_dot8_i32_i4 v40, v77, v1, v40
	v_dot8_i32_i4 v35, v73, v3, v35
	v_dot8_i32_i4 v36, v77, v3, v36
	v_dot8_i32_i4 v39, v74, v44, v39
	v_dot8_i32_i4 v40, v78, v44, v40
	v_dot8_i32_i4 v35, v74, v46, v35
	v_dot8_i32_i4 v36, v78, v46, v36
	v_dot8_i32_i4 v39, v75, v45, v39
	v_dot8_i32_i4 v40, v79, v45, v40
	v_dot8_i32_i4 v35, v75, v47, v35
	v_dot8_i32_i4 v36, v79, v47, v36
	s_nop 2
	v_lshl_add_u32 v39, v39, 4, v35
	v_lshl_add_u32 v40, v40, 4, v36
	s_mulk_i32 s1, 0x690
	s_nop 0
	v_permlane16_swap_b32_e32 v39, v40
	v_add_u32_e32 v39, v39, v40
	s_lshr_b32 s4, s15, 17
	s_add_i32 s1, s90, s1
	v_add_u32_dpp v39, v39, v39 quad_perm:[1,0,3,2] row_mask:0xf bank_mask:0xf bound_ctrl:1
	s_and_b32 s4, s4, 0x7ffc
	s_add_i32 s1, s1, s4
	v_add_u32_dpp v39, v39, v39 quad_perm:[2,3,0,1] row_mask:0xf bank_mask:0xf bound_ctrl:1
	v_lshl_add_u32 v34, v33, 2, s1
	s_nop 0
	v_add_u32_dpp v41, v39, v39 row_half_mirror row_mask:0xf bank_mask:0xf bound_ctrl:1
	s_nop 1
	v_mov_b32_dpp v42, v41 row_mirror row_mask:0xf bank_mask:0xf bound_ctrl:1
	v_add_u32_e32 v42, v41, v42
	s_and_saveexec_b64 s[0:1], vcc
	ds_write_b32 v34, v42
	s_or_b64 exec, exec, s[0:1]
.Lu16_skip5:
	s_waitcnt lgkmcnt(0)
	v_readfirstlane_b32 s15, v4
	v_and_b32_e32 v48, 0x3fff, v4
	v_cndmask_b32_e64 v48, v48, v5, s[100:101]
	v_lshl_add_u32 v48, v48, 9, v43
	global_load_dwordx4 v[72:75], v48, s[70:71]
	v_cndmask_b32_e64 v48, v6, v7, s[100:101]
	v_lshl_add_u32 v48, v48, 9, v43
	global_load_dwordx4 v[76:79], v48, s[70:71]
	s_add_i32 s7, s7, 6
	s_add_i32 s8, s8, 96
	v_add_u32_e32 v136, 96, v136
	s_cmp_ge_i32 s7, s6
	s_cbranch_scc0 .LBB0_2838
